# pipelined attention: softmax VALU paced by issue weight (exp=2, others=1), at most ~8 issue cycles per MFMA gap
# speedup vs baseline: 1.0118x; 1.0102x over previous
.LBB0_733:
	s_or_b64 exec, exec, s[8:9]
	s_movk_i32 s4, 0xf0
	s_cmp_lg_u32 0, -1
	v_lshlrev_b32_e32 v39, 8, v141
	v_bitop3_b32 v80, v142, s4, v136 bitop3:0x48
	s_cselect_b32 s10, 0, 0
	v_cvt_pk_bf16_f32 v96, v134, v135
	v_cvt_pk_bf16_f32 v97, v132, v133
	v_cvt_pk_bf16_f32 v98, v130, v131
	v_cvt_pk_bf16_f32 v99, v128, v129
	v_cvt_pk_bf16_f32 v100, v126, v127
	v_cvt_pk_bf16_f32 v101, v124, v125
	v_cvt_pk_bf16_f32 v102, v122, v123
	v_cvt_pk_bf16_f32 v103, v120, v121
	v_cvt_pk_bf16_f32 v104, v70, v71
	v_cvt_pk_bf16_f32 v105, v74, v75
	v_cvt_pk_bf16_f32 v106, v64, v65
	v_cvt_pk_bf16_f32 v107, v68, v69
	v_cvt_pk_bf16_f32 v108, v60, v61
	v_cvt_pk_bf16_f32 v109, v66, v67
	v_cvt_pk_bf16_f32 v110, v56, v57
	v_cvt_pk_bf16_f32 v111, v58, v59
	v_cvt_pk_bf16_f32 v112, v112, v113
	v_cvt_pk_bf16_f32 v113, v118, v119
	v_cvt_pk_bf16_f32 v114, v114, v115
	v_cvt_pk_bf16_f32 v115, v116, v117
	v_cvt_pk_bf16_f32 v116, v78, v79
	v_cvt_pk_bf16_f32 v117, v76, v77
	v_cvt_pk_bf16_f32 v118, v72, v73
	v_cvt_pk_bf16_f32 v119, v62, v63
	v_cvt_pk_bf16_f32 v120, v52, v53
	v_cvt_pk_bf16_f32 v121, v54, v55
	v_cvt_pk_bf16_f32 v122, v46, v47
	v_cvt_pk_bf16_f32 v123, v50, v51
	v_cvt_pk_bf16_f32 v124, v44, v45
	v_cvt_pk_bf16_f32 v125, v48, v49
	v_cvt_pk_bf16_f32 v126, v40, v41
	v_cvt_pk_bf16_f32 v127, v42, v43
	v_readlane_b32 s100, v250, 8
	v_mbcnt_lo_u32_b32 v68, -1, 0
	v_mbcnt_hi_u32_b32 v68, -1, v68
	s_nop 1
	v_add_u32_e32 v69, s100, v68
	v_lshrrev_b32_e32 v70, 3, v69
	v_and_b32_e32 v71, 7, v69
	v_lshrrev_b32_e32 v72, 2, v71
	v_bfe_u32 v73, v71, 1, 1
	v_and_b32_e32 v74, 1, v71
	v_lshlrev_b32_e32 v74, 1, v74
	v_lshl_add_u32 v75, v72, 2, v74
	v_bfe_u32 v76, v70, 1, 3
	v_xor_b32_e32 v77, v75, v76
	v_add_u32_e32 v78, 1, v75
	v_xor_b32_e32 v78, v78, v76
	v_lshlrev_b32_e32 v79, 7, v70
	v_lshl_add_u32 v79, v73, 3, v79
	v_lshl_add_u32 v64, v77, 4, v79
	v_lshl_add_u32 v65, v78, 4, v79
	v_add_u32_e32 v66, 0x2000, v64
	v_add_u32_e32 v67, 0x2000, v65
	v_or_b32_e32 v81, v39, v80
	s_add_i32 s15, s10, 0x10000
	v_and_b32_e32 v82, 6, v137
	v_lshrrev_b32_e32 v84, 4, v136
	s_waitcnt vmcnt(0)
	s_waitcnt vmcnt(0)
	s_add_i32 s11, s10, 0x12000
	v_lshl_add_u32 v83, v139, 7, s10
	v_bitop3_b32 v85, v84, v82, 7 bitop3:0x6c
	v_and_b32_e32 v86, 8, v138
	v_or_b32_e32 v82, 1, v82
	v_add_u32_e32 v225, s15, v81
	s_waitcnt vmcnt(4)
	ds_write_b128 v225, v[24:27] offset:0
	v_lshlrev_b32_e32 v85, 4, v85
	v_add_u32_e32 v87, v83, v86
	v_bitop3_b32 v82, v84, v82, 7 bitop3:0x6c
	v_add3_u32 v226, v80, s11, v39
	ds_write_b128 v226, v[28:31] offset:0
	v_lshlrev_b32_e32 v82, 4, v82
	v_add_u32_e32 v227, v87, v85
	ds_write_b64 v64, v[12:13] offset:0
	v_lshrrev_b32_e32 v32, 5, v136
	v_add_u32_e32 v83, 0x2000, v83
	v_or_b32_e32 v84, v85, v86
	v_add_u32_e32 v228, v87, v82
	ds_write_b64 v65, v[14:15] offset:0
	v_xor_b32_e32 v32, v32, v137
	v_or_b32_e32 v86, v82, v86
	v_add_u32_e32 v229, v84, v83
	ds_write_b64 v66, v[4:5] offset:0
	v_lshlrev_b32_e32 v32, 4, v32
	v_add_u32_e32 v184, v86, v83
	ds_write_b64 v67, v[6:7] offset:0
	v_lshlrev_b32_e32 v33, 8, v143
	v_and_b32_e32 v32, 16, v32
	v_bfe_u32 v35, v137, 1, 3
	s_waitcnt vmcnt(4)
	ds_write_b128 v225, v[20:23] offset:0x4000
	v_lshlrev_b32_e32 v36, 5, v35
	v_add3_u32 v32, v33, s15, v32
	s_movk_i32 s16, 0x60
	ds_write_b128 v226, v[16:19] offset:0x4000
	v_xad_u32 v204, v36, s16, v32
	s_movk_i32 s16, 0x80
	ds_write_b64 v64, v[8:9] offset:0x4000
	v_xad_u32 v205, v36, s16, v32
	s_movk_i32 s16, 0xa0
	ds_write_b64 v65, v[10:11] offset:0x4000
	s_add_u32 s8, s6, 0x100
	v_xad_u32 v206, v36, s16, v32
	s_movk_i32 s16, 0xc0
	ds_write_b64 v66, v[0:1] offset:0x4000
	s_addc_u32 s9, s7, 0
	v_xad_u32 v207, v36, s16, v32
	s_movk_i32 s16, 0xe0
	ds_write_b64 v67, v[2:3] offset:0x4000
	v_add_u32_e32 v201, v32, v36
	v_xad_u32 v202, v36, 32, v32
	v_xad_u32 v203, v36, 64, v32
	v_xad_u32 v208, v36, s16, v32
	v_lshl_add_u32 v32, v143, 7, s10
	s_add_u32 s10, s78, 0x20000
	global_load_dwordx4 v[132:135], v198, s[8:9]
	s_addc_u32 s11, s79, 0
	global_load_dwordx4 v[128:131], v199, s[8:9]
	v_lshrrev_b32_e32 v34, 1, v137
	global_load_dwordx4 v[136:139], v196, s[10:11]
	s_add_u32 s6, s6, 0x180
	v_bitop3_b32 v34, v140, v34, 7 bitop3:0x78
	v_bitop3_b32 v37, v140, v35, 2 bitop3:0x36
	v_bitop3_b32 v38, v140, v35, 4 bitop3:0x36
	v_bitop3_b32 v35, v140, v35, 6 bitop3:0x36
	global_load_dwordx4 v[140:143], v197, s[10:11]
	s_addc_u32 s7, s7, 0
	s_add_u32 s8, s78, 0x30000
	global_load_dwordx4 v[148:151], v198, s[6:7]
	s_addc_u32 s9, s79, 0
	global_load_dwordx4 v[144:147], v199, s[6:7]
	global_load_dwordx4 v[152:155], v196, s[8:9]
	s_add_u32 s10, s13, s14
	global_load_dwordx4 v[156:159], v197, s[8:9]
	s_addc_u32 s11, s12, 0
	s_add_u32 s12, s41, s30
	v_mov_b32_e32 v0, 0
	s_mov_b32 s4, 0
	v_lshl_add_u32 v209, v34, 4, v32
	v_lshl_add_u32 v210, v37, 4, v32
	v_lshl_add_u32 v211, v38, 4, v32
	v_lshl_add_u32 v224, v35, 4, v32
	s_addc_u32 s13, 0, s31
	v_mov_b32_e32 v1, v0
	v_mov_b32_e32 v2, v0
	v_mov_b32_e32 v3, v0
	v_mov_b32_e32 v4, v0
	v_mov_b32_e32 v5, v0
	v_mov_b32_e32 v6, v0
	v_mov_b32_e32 v7, v0
	v_mov_b32_e32 v8, v0
	v_mov_b32_e32 v9, v0
	v_mov_b32_e32 v10, v0
	v_mov_b32_e32 v11, v0
	v_mov_b32_e32 v12, v0
	v_mov_b32_e32 v13, v0
	v_mov_b32_e32 v14, v0
	v_mov_b32_e32 v15, v0
	v_mov_b32_e32 v16, v0
	v_mov_b32_e32 v17, v0
	v_mov_b32_e32 v18, v0
	v_mov_b32_e32 v19, v0
	v_mov_b32_e32 v20, v0
	v_mov_b32_e32 v21, v0
	v_mov_b32_e32 v22, v0
	v_mov_b32_e32 v23, v0
	v_mov_b32_e32 v24, v0
	v_mov_b32_e32 v25, v0
	v_mov_b32_e32 v26, v0
	v_mov_b32_e32 v27, v0
	v_mov_b32_e32 v28, v0
	v_mov_b32_e32 v29, v0
	v_mov_b32_e32 v30, v0
	v_mov_b32_e32 v31, v0
	v_mov_b32_e32 v32, v0
	v_mov_b32_e32 v33, v0
	v_mov_b32_e32 v34, v0
	v_mov_b32_e32 v35, v0
	v_mov_b32_e32 v36, v0
	v_mov_b32_e32 v37, v0
	v_mov_b32_e32 v38, v0
	v_mov_b32_e32 v39, v0
	v_mov_b32_e32 v40, v0
	v_mov_b32_e32 v41, v0
	v_mov_b32_e32 v42, v0
	v_mov_b32_e32 v43, v0
	v_mov_b32_e32 v44, v0
	v_mov_b32_e32 v45, v0
	v_mov_b32_e32 v46, v0
	v_mov_b32_e32 v47, v0
	v_mov_b32_e32 v48, v0
	v_mov_b32_e32 v49, v0
	v_mov_b32_e32 v50, v0
	v_mov_b32_e32 v51, v0
	v_mov_b32_e32 v52, v0
	v_mov_b32_e32 v53, v0
	v_mov_b32_e32 v54, v0
	v_mov_b32_e32 v55, v0
	v_mov_b32_e32 v56, v0
	v_mov_b32_e32 v57, v0
	v_mov_b32_e32 v58, v0
	v_mov_b32_e32 v59, v0
	v_mov_b32_e32 v60, v0
	v_mov_b32_e32 v61, v0
	v_mov_b32_e32 v62, v0
	v_mov_b32_e32 v63, v0
	v_mov_b32_e32 v160, v0
	v_mov_b32_e32 v161, v0
	v_mov_b32_e32 v227, v64
	v_mov_b32_e32 v228, v65
	v_mov_b32_e32 v229, v66
	v_mov_b32_e32 v184, v67
	v_readlane_b32 s100, v250, 8
	v_mbcnt_lo_u32_b32 v68, -1, 0
	v_mbcnt_hi_u32_b32 v68, -1, v68
	v_and_b32_e32 v69, 15, v68
	v_lshrrev_b32_e32 v70, 4, v68
	v_lshlrev_b32_e32 v72, 8, v69
	v_add_u32_e32 v72, 0x10000, v72
	v_add_u32_e32 v71, 0, v70
	v_xor_b32_e32 v71, v71, v69
	v_lshl_add_u32 v201, v71, 4, v72
	v_add_u32_e32 v71, 4, v70
	v_xor_b32_e32 v71, v71, v69
	v_lshl_add_u32 v202, v71, 4, v72
	v_add_u32_e32 v71, 8, v70
	v_xor_b32_e32 v71, v71, v69
	v_lshl_add_u32 v203, v71, 4, v72
	v_add_u32_e32 v71, 12, v70
	v_xor_b32_e32 v71, v71, v69
	v_lshl_add_u32 v246, v71, 4, v72
	v_bfe_u32 v73, v69, 1, 3
	v_lshlrev_b32_e32 v76, 7, v69
	v_add_u32_e32 v71, 0, v70
	v_xor_b32_e32 v71, v71, v73
	v_lshl_add_u32 v209, v71, 4, v76
	v_add_u32_e32 v71, 4, v70
	v_xor_b32_e32 v71, v71, v73
	v_lshl_add_u32 v210, v71, 4, v76
	s_lshl_b32 s101, s100, 7
	s_add_u32 s101, s101, 0x8000
	s_cmpk_ge_u32 s100, 0x100
	s_cselect_b32 s6, 0x8000, 0
	s_add_u32 s101, s101, s6
	v_and_b32_e32 v74, 31, v68
	v_lshrrev_b32_e32 v75, 5, v68
	v_lshlrev_b32_e32 v74, 8, v74
	v_lshl_add_u32 v74, v75, 4, v74
	v_add_u32_e32 v74, s101, v74
	v_lshlrev_b32_e32 v75, 8, v69
	v_lshl_add_u32 v75, v70, 4, v75
	v_add_u32_e32 v75, s101, v75
	ds_write_b128 v74, v[96:99] offset:0
	ds_write_b128 v74, v[100:103] offset:32
	ds_write_b128 v74, v[104:107] offset:64
	ds_write_b128 v74, v[108:111] offset:96
	ds_write_b128 v74, v[112:115] offset:128
	ds_write_b128 v74, v[116:119] offset:160
	ds_write_b128 v74, v[120:123] offset:192
	ds_write_b128 v74, v[124:127] offset:224
	s_waitcnt lgkmcnt(0)
	ds_read_b128 v[96:99], v75 offset:0
	ds_read_b128 v[100:103], v75 offset:64
	ds_read_b128 v[104:107], v75 offset:128
	ds_read_b128 v[108:111], v75 offset:192
	ds_read_b128 v[112:115], v75 offset:4096
	ds_read_b128 v[116:119], v75 offset:4160
	ds_read_b128 v[120:123], v75 offset:4224
	ds_read_b128 v[124:127], v75 offset:4288
	s_waitcnt vmcnt(0)
	s_waitcnt lgkmcnt(0)
	s_barrier
	ds_write_b128 v225, v[136:139] offset:32768
	ds_write_b128 v226, v[140:143] offset:32768
	s_add_u32 s15, s22, s12
	s_addc_u32 s14, s23, s13
	s_add_u32 s6, s15, 0x23a40000
	s_addc_u32 s7, s14, 0
	s_waitcnt lgkmcnt(0)
	global_load_dwordx4 v[136:139], v196, s[6:7]
	global_load_dwordx4 v[140:143], v197, s[6:7]
	v_mov_b32_e32 v194, 0
	v_mov_b32_e32 v195, 0
	s_barrier
	ds_read_b128 v[160:163], v201 offset:0
	ds_read_b128 v[164:167], v202 offset:0
	ds_read_b128 v[168:171], v203 offset:0
	ds_read_b128 v[172:175], v246 offset:0
	ds_read_b128 v[176:179], v201 offset:4096
	ds_read_b128 v[180:183], v202 offset:4096
	ds_read_b128 v[230:233], v203 offset:4096
	s_waitcnt lgkmcnt(6)
	v_mfma_f32_16x16x32_bf16 v[64:67], v[160:163], v[96:99], 0
	v_mfma_f32_16x16x32_bf16 v[68:71], v[160:163], v[112:115], 0
	ds_read_b128 v[234:237], v246 offset:4096
	s_waitcnt lgkmcnt(6)
	v_mfma_f32_16x16x32_bf16 v[68:71], v[164:167], v[116:119], v[68:71]
	v_mfma_f32_16x16x32_bf16 v[64:67], v[164:167], v[100:103], v[64:67]
	ds_read_b128 v[160:163], v201 offset:8192
	s_waitcnt lgkmcnt(6)
	v_mfma_f32_16x16x32_bf16 v[64:67], v[168:171], v[104:107], v[64:67]
	v_mfma_f32_16x16x32_bf16 v[68:71], v[168:171], v[120:123], v[68:71]
	ds_read_b128 v[164:167], v202 offset:8192
	s_waitcnt lgkmcnt(6)
	v_mfma_f32_16x16x32_bf16 v[68:71], v[172:175], v[124:127], v[68:71]
	v_mfma_f32_16x16x32_bf16 v[64:67], v[172:175], v[108:111], v[64:67]
	ds_read_b128 v[168:171], v203 offset:8192
	s_waitcnt lgkmcnt(6)
	v_mfma_f32_16x16x32_bf16 v[72:75], v[176:179], v[96:99], 0
	s_nop 7
	s_nop 1
	v_exp_f32_e32 v64, v64
	v_mfma_f32_16x16x32_bf16 v[76:79], v[176:179], v[112:115], 0
	v_exp_f32_e32 v68, v68
	ds_read_b128 v[172:175], v246 offset:8192
	s_waitcnt lgkmcnt(6)
	v_mfma_f32_16x16x32_bf16 v[76:79], v[180:183], v[116:119], v[76:79]
	v_exp_f32_e32 v65, v65
	v_exp_f32_e32 v69, v69
	v_mfma_f32_16x16x32_bf16 v[72:75], v[180:183], v[100:103], v[72:75]
	v_exp_f32_e32 v66, v66
	ds_read_b128 v[176:179], v201 offset:12288
	s_waitcnt lgkmcnt(6)
	v_mfma_f32_16x16x32_bf16 v[72:75], v[230:233], v[104:107], v[72:75]
	v_exp_f32_e32 v70, v70
	v_exp_f32_e32 v67, v67
	v_mfma_f32_16x16x32_bf16 v[76:79], v[230:233], v[120:123], v[76:79]
	v_exp_f32_e32 v71, v71
	v_add_f32_e32 v220, v64, v65
	ds_read_b128 v[180:183], v202 offset:12288
	s_waitcnt lgkmcnt(6)
	v_mfma_f32_16x16x32_bf16 v[76:79], v[234:237], v[124:127], v[76:79]
	v_add_f32_e32 v221, v68, v69
	v_add_f32_e32 v220, v220, v66
	v_add_f32_e32 v221, v221, v70
	v_mfma_f32_16x16x32_bf16 v[72:75], v[234:237], v[108:111], v[72:75]
	v_add_f32_e32 v220, v220, v67
	v_add_f32_e32 v221, v221, v71
	ds_read_b128 v[230:233], v203 offset:12288
	s_waitcnt lgkmcnt(6)
	v_mfma_f32_16x16x32_bf16 v[80:83], v[160:163], v[96:99], 0
	s_nop 7
	s_nop 1
	v_exp_f32_e32 v72, v72
	v_exp_f32_e32 v76, v76
	v_mfma_f32_16x16x32_bf16 v[84:87], v[160:163], v[112:115], 0
	v_exp_f32_e32 v73, v73
	v_exp_f32_e32 v77, v77
	ds_read_b128 v[234:237], v246 offset:12288
	s_waitcnt lgkmcnt(6)
	v_mfma_f32_16x16x32_bf16 v[84:87], v[164:167], v[116:119], v[84:87]
	v_exp_f32_e32 v74, v74
	v_exp_f32_e32 v78, v78
	v_mfma_f32_16x16x32_bf16 v[80:83], v[164:167], v[100:103], v[80:83]
	v_exp_f32_e32 v75, v75
	v_exp_f32_e32 v79, v79
	s_waitcnt lgkmcnt(5)
	v_mfma_f32_16x16x32_bf16 v[80:83], v[168:171], v[104:107], v[80:83]
	v_add_f32_e32 v220, v220, v72
	v_add_f32_e32 v221, v221, v76
	v_add_f32_e32 v220, v220, v73
	v_add_f32_e32 v221, v221, v77
	v_mfma_f32_16x16x32_bf16 v[84:87], v[168:171], v[120:123], v[84:87]
	v_add_f32_e32 v220, v220, v74
	v_add_f32_e32 v221, v221, v78
	v_add_f32_e32 v220, v220, v75
	v_add_f32_e32 v221, v221, v79
	s_waitcnt lgkmcnt(4)
	v_mfma_f32_16x16x32_bf16 v[84:87], v[172:175], v[124:127], v[84:87]
	v_cvt_pk_bf16_f32 v216, v64, v65
	v_cvt_pk_bf16_f32 v217, v66, v67
	v_cvt_pk_bf16_f32 v238, v68, v69
	v_cvt_pk_bf16_f32 v239, v70, v71
	v_mfma_f32_16x16x32_bf16 v[80:83], v[172:175], v[108:111], v[80:83]
	v_cvt_pk_bf16_f32 v218, v72, v73
	v_cvt_pk_bf16_f32 v219, v74, v75
	v_cvt_pk_bf16_f32 v240, v76, v77
	v_cvt_pk_bf16_f32 v241, v78, v79
	s_waitcnt lgkmcnt(3)
	v_mfma_f32_16x16x32_bf16 v[88:91], v[176:179], v[96:99], 0
	s_nop 7
	s_nop 1
	v_exp_f32_e32 v80, v80
	v_exp_f32_e32 v84, v84
	v_mfma_f32_16x16x32_bf16 v[92:95], v[176:179], v[112:115], 0
	v_exp_f32_e32 v81, v81
	s_waitcnt lgkmcnt(2)
	v_mfma_f32_16x16x32_bf16 v[92:95], v[180:183], v[116:119], v[92:95]
	v_exp_f32_e32 v85, v85
	v_exp_f32_e32 v82, v82
	v_mfma_f32_16x16x32_bf16 v[88:91], v[180:183], v[100:103], v[88:91]
	v_exp_f32_e32 v86, v86
	s_waitcnt lgkmcnt(1)
	v_mfma_f32_16x16x32_bf16 v[88:91], v[230:233], v[104:107], v[88:91]
	v_exp_f32_e32 v83, v83
	v_exp_f32_e32 v87, v87
	v_mfma_f32_16x16x32_bf16 v[92:95], v[230:233], v[120:123], v[92:95]
	v_add_f32_e32 v220, v220, v80
	v_add_f32_e32 v221, v221, v84
	v_add_f32_e32 v220, v220, v81
	s_waitcnt lgkmcnt(0)
	v_mfma_f32_16x16x32_bf16 v[92:95], v[234:237], v[124:127], v[92:95]
	v_add_f32_e32 v221, v221, v85
	v_add_f32_e32 v220, v220, v82
	v_add_f32_e32 v221, v221, v86
	v_mfma_f32_16x16x32_bf16 v[88:91], v[234:237], v[108:111], v[88:91]
	v_add_f32_e32 v220, v220, v83
	v_add_f32_e32 v221, v221, v87
.LBB0_734:
	s_waitcnt lgkmcnt(0)
	s_barrier
	ds_read_b128 v[160:163], v201 offset:16384
	ds_read_b128 v[164:167], v209 offset:0
	ds_read_b128 v[168:171], v202 offset:16384
	ds_read_b128 v[172:175], v209 offset:2048
	ds_read_b128 v[176:179], v203 offset:16384
	ds_read_b128 v[180:183], v209 offset:4096
	ds_read_b128 v[230:233], v246 offset:16384
	s_waitcnt lgkmcnt(6)
	v_mfma_f32_16x16x32_bf16 v[64:67], v[160:163], v[96:99], 0
	v_exp_f32_e32 v88, v88
	v_mfma_f32_16x16x32_bf16 v[68:71], v[160:163], v[112:115], 0
	v_exp_f32_e32 v92, v92
	ds_read_b128 v[234:237], v209 offset:6144
	s_add_u32 s16, s22, s10
	s_addc_u32 s17, s23, s11
	s_add_u32 s15, s22, s12
	s_addc_u32 s14, s23, s13
	s_add_u32 s8, s16, 0x3bc00200
	s_addc_u32 s9, s17, 0
	s_add_u32 s6, s15, 0x23a50000
	s_addc_u32 s7, s14, 0
	s_waitcnt lgkmcnt(6)
	v_mfma_f32_16x16x32_bf16 v[0:3], v[164:167], v[216:219], v[0:3]
	v_cvt_pk_bf16_f32 v242, v80, v81
	v_mfma_f32_16x16x32_bf16 v[4:7], v[164:167], v[238:241], v[4:7]
	v_exp_f32_e32 v89, v89
	ds_read_b128 v[160:163], v201 offset:20480
	s_waitcnt vmcnt(4)
	ds_write_b128 v225, v[152:155] offset:49152
	s_waitcnt lgkmcnt(7)
	v_mfma_f32_16x16x32_bf16 v[68:71], v[168:171], v[116:119], v[68:71]
	v_exp_f32_e32 v93, v93
	v_mfma_f32_16x16x32_bf16 v[64:67], v[168:171], v[100:103], v[64:67]
	v_cvt_pk_bf16_f32 v243, v82, v83
	ds_read_b128 v[164:167], v209 offset:8192
	ds_write_b128 v226, v[156:159] offset:49152
	s_waitcnt lgkmcnt(8)
	v_mfma_f32_16x16x32_bf16 v[12:15], v[172:175], v[238:241], v[12:15]
	v_exp_f32_e32 v90, v90
	v_mfma_f32_16x16x32_bf16 v[8:11], v[172:175], v[216:219], v[8:11]
	v_exp_f32_e32 v94, v94
	ds_read_b128 v[168:171], v202 offset:20480
	ds_write_b64 v227, v[132:133] offset:32768
	s_waitcnt lgkmcnt(9)
	v_mfma_f32_16x16x32_bf16 v[64:67], v[176:179], v[104:107], v[64:67]
	v_cvt_pk_bf16_f32 v204, v84, v85
	v_mfma_f32_16x16x32_bf16 v[68:71], v[176:179], v[120:123], v[68:71]
	v_exp_f32_e32 v91, v91
	ds_read_b128 v[172:175], v209 offset:10240
	ds_write_b64 v228, v[134:135] offset:32768
	s_waitcnt lgkmcnt(10)
	v_mfma_f32_16x16x32_bf16 v[16:19], v[180:183], v[216:219], v[16:19]
	v_exp_f32_e32 v95, v95
	v_mfma_f32_16x16x32_bf16 v[20:23], v[180:183], v[238:241], v[20:23]
	v_cvt_pk_bf16_f32 v205, v86, v87
	v_add_f32_e32 v220, v220, v88
	ds_read_b128 v[176:179], v203 offset:20480
	ds_write_b64 v229, v[128:129] offset:32768
	s_waitcnt lgkmcnt(11)
	v_mfma_f32_16x16x32_bf16 v[68:71], v[230:233], v[124:127], v[68:71]
	v_add_f32_e32 v221, v221, v92
	v_add_f32_e32 v220, v220, v89
	v_mfma_f32_16x16x32_bf16 v[64:67], v[230:233], v[108:111], v[64:67]
	v_add_f32_e32 v221, v221, v93
	v_cvt_pk_bf16_f32 v244, v88, v89
	ds_read_b128 v[180:183], v209 offset:12288
	ds_write_b64 v184, v[130:131] offset:32768
	s_waitcnt lgkmcnt(12)
	v_mfma_f32_16x16x32_bf16 v[28:31], v[234:237], v[238:241], v[28:31]
	v_cvt_pk_bf16_f32 v245, v90, v91
	v_cvt_pk_bf16_f32 v206, v92, v93
	v_mfma_f32_16x16x32_bf16 v[24:27], v[234:237], v[216:219], v[24:27]
	v_cvt_pk_bf16_f32 v207, v94, v95
	ds_read_b128 v[230:233], v246 offset:20480
	global_load_dwordx4 v[132:135], v198, s[8:9]
	s_waitcnt lgkmcnt(12)
	v_mfma_f32_16x16x32_bf16 v[72:75], v[160:163], v[96:99], 0
	v_add_f32_e32 v220, v220, v90
	v_add_f32_e32 v221, v221, v94
	v_mfma_f32_16x16x32_bf16 v[76:79], v[160:163], v[112:115], 0
	v_add_f32_e32 v220, v220, v91
	v_add_f32_e32 v221, v221, v95
	ds_read_b128 v[234:237], v209 offset:14336
	global_load_dwordx4 v[128:131], v199, s[8:9]
	s_waitcnt lgkmcnt(11)
	v_mfma_f32_16x16x32_bf16 v[32:35], v[164:167], v[216:219], v[32:35]
	v_add_f32_e32 v194, v194, v220
	v_add_f32_e32 v195, v195, v221
	v_mfma_f32_16x16x32_bf16 v[36:39], v[164:167], v[238:241], v[36:39]
	v_exp_f32_e32 v64, v64
	ds_read_b128 v[160:163], v201 offset:24576
	global_load_dwordx4 v[152:155], v196, s[6:7]
	s_waitcnt lgkmcnt(10)
	v_mfma_f32_16x16x32_bf16 v[76:79], v[168:171], v[116:119], v[76:79]
	v_exp_f32_e32 v68, v68
	v_mfma_f32_16x16x32_bf16 v[72:75], v[168:171], v[100:103], v[72:75]
	v_exp_f32_e32 v65, v65
	ds_read_b128 v[164:167], v210 offset:0
	global_load_dwordx4 v[156:159], v197, s[6:7]
	s_waitcnt lgkmcnt(9)
	v_mfma_f32_16x16x32_bf16 v[44:47], v[172:175], v[238:241], v[44:47]
	v_exp_f32_e32 v69, v69
	v_mfma_f32_16x16x32_bf16 v[40:43], v[172:175], v[216:219], v[40:43]
	v_exp_f32_e32 v66, v66
	ds_read_b128 v[168:171], v202 offset:24576
	s_waitcnt lgkmcnt(8)
	v_mfma_f32_16x16x32_bf16 v[72:75], v[176:179], v[104:107], v[72:75]
	v_exp_f32_e32 v70, v70
	v_mfma_f32_16x16x32_bf16 v[76:79], v[176:179], v[120:123], v[76:79]
	v_exp_f32_e32 v67, v67
	ds_read_b128 v[172:175], v210 offset:2048
	s_waitcnt lgkmcnt(7)
	v_mfma_f32_16x16x32_bf16 v[48:51], v[180:183], v[216:219], v[48:51]
	v_exp_f32_e32 v71, v71
	v_mfma_f32_16x16x32_bf16 v[52:55], v[180:183], v[238:241], v[52:55]
	v_add_f32_e32 v220, v64, v65
	ds_read_b128 v[176:179], v203 offset:24576
	s_waitcnt lgkmcnt(6)
	v_mfma_f32_16x16x32_bf16 v[76:79], v[230:233], v[124:127], v[76:79]
	v_add_f32_e32 v221, v68, v69
	v_mfma_f32_16x16x32_bf16 v[72:75], v[230:233], v[108:111], v[72:75]
	v_add_f32_e32 v220, v220, v66
	ds_read_b128 v[180:183], v210 offset:4096
	s_waitcnt lgkmcnt(6)
	v_mfma_f32_16x16x32_bf16 v[60:63], v[234:237], v[238:241], v[60:63]
	v_add_f32_e32 v221, v221, v70
	v_add_f32_e32 v220, v220, v67
	v_mfma_f32_16x16x32_bf16 v[56:59], v[234:237], v[216:219], v[56:59]
	v_add_f32_e32 v221, v221, v71
	ds_read_b128 v[230:233], v246 offset:24576
	s_waitcnt lgkmcnt(6)
	v_mfma_f32_16x16x32_bf16 v[80:83], v[160:163], v[96:99], 0
	v_exp_f32_e32 v72, v72
	v_mfma_f32_16x16x32_bf16 v[84:87], v[160:163], v[112:115], 0
	v_exp_f32_e32 v76, v76
	ds_read_b128 v[234:237], v210 offset:6144
	s_waitcnt lgkmcnt(6)
	v_mfma_f32_16x16x32_bf16 v[0:3], v[164:167], v[242:245], v[0:3]
	v_exp_f32_e32 v73, v73
	v_mfma_f32_16x16x32_bf16 v[4:7], v[164:167], v[204:207], v[4:7]
	v_exp_f32_e32 v77, v77
	ds_read_b128 v[160:163], v201 offset:28672
	s_waitcnt lgkmcnt(6)
	v_mfma_f32_16x16x32_bf16 v[84:87], v[168:171], v[116:119], v[84:87]
	v_exp_f32_e32 v74, v74
	v_mfma_f32_16x16x32_bf16 v[80:83], v[168:171], v[100:103], v[80:83]
	v_exp_f32_e32 v78, v78
	ds_read_b128 v[164:167], v210 offset:8192
	s_waitcnt lgkmcnt(6)
	v_mfma_f32_16x16x32_bf16 v[12:15], v[172:175], v[204:207], v[12:15]
	v_exp_f32_e32 v75, v75
	v_mfma_f32_16x16x32_bf16 v[8:11], v[172:175], v[242:245], v[8:11]
	v_exp_f32_e32 v79, v79
	ds_read_b128 v[168:171], v202 offset:28672
	s_waitcnt lgkmcnt(6)
	v_mfma_f32_16x16x32_bf16 v[80:83], v[176:179], v[104:107], v[80:83]
	v_add_f32_e32 v220, v220, v72
	v_add_f32_e32 v221, v221, v76
	v_mfma_f32_16x16x32_bf16 v[84:87], v[176:179], v[120:123], v[84:87]
	v_add_f32_e32 v220, v220, v73
	ds_read_b128 v[172:175], v210 offset:10240
	s_waitcnt lgkmcnt(6)
	v_mfma_f32_16x16x32_bf16 v[16:19], v[180:183], v[242:245], v[16:19]
	v_add_f32_e32 v221, v221, v77
	v_add_f32_e32 v220, v220, v74
	v_mfma_f32_16x16x32_bf16 v[20:23], v[180:183], v[204:207], v[20:23]
	v_add_f32_e32 v221, v221, v78
	ds_read_b128 v[176:179], v203 offset:28672
	s_waitcnt lgkmcnt(6)
	v_mfma_f32_16x16x32_bf16 v[84:87], v[230:233], v[124:127], v[84:87]
	v_add_f32_e32 v220, v220, v75
	v_add_f32_e32 v221, v221, v79
	v_mfma_f32_16x16x32_bf16 v[80:83], v[230:233], v[108:111], v[80:83]
	v_cvt_pk_bf16_f32 v216, v64, v65
	ds_read_b128 v[180:183], v210 offset:12288
	s_waitcnt lgkmcnt(6)
	v_mfma_f32_16x16x32_bf16 v[28:31], v[234:237], v[204:207], v[28:31]
	v_cvt_pk_bf16_f32 v217, v66, v67
	v_cvt_pk_bf16_f32 v238, v68, v69
	v_mfma_f32_16x16x32_bf16 v[24:27], v[234:237], v[242:245], v[24:27]
	v_cvt_pk_bf16_f32 v239, v70, v71
	ds_read_b128 v[230:233], v246 offset:28672
	s_waitcnt lgkmcnt(6)
	v_mfma_f32_16x16x32_bf16 v[88:91], v[160:163], v[96:99], 0
	v_exp_f32_e32 v80, v80
	v_mfma_f32_16x16x32_bf16 v[92:95], v[160:163], v[112:115], 0
	v_exp_f32_e32 v84, v84
	ds_read_b128 v[234:237], v210 offset:14336
	s_waitcnt lgkmcnt(6)
	v_mfma_f32_16x16x32_bf16 v[32:35], v[164:167], v[242:245], v[32:35]
	v_exp_f32_e32 v81, v81
	v_mfma_f32_16x16x32_bf16 v[36:39], v[164:167], v[204:207], v[36:39]
	v_exp_f32_e32 v85, v85
	ds_read_b128 v[160:163], v201 offset:32768
	s_waitcnt lgkmcnt(6)
	v_mfma_f32_16x16x32_bf16 v[92:95], v[168:171], v[116:119], v[92:95]
	v_exp_f32_e32 v82, v82
	v_mfma_f32_16x16x32_bf16 v[88:91], v[168:171], v[100:103], v[88:91]
	v_exp_f32_e32 v86, v86
	ds_read_b128 v[164:167], v209 offset:16384
	s_waitcnt lgkmcnt(6)
	v_mfma_f32_16x16x32_bf16 v[44:47], v[172:175], v[204:207], v[44:47]
	v_exp_f32_e32 v83, v83
	v_mfma_f32_16x16x32_bf16 v[40:43], v[172:175], v[242:245], v[40:43]
	v_exp_f32_e32 v87, v87
	ds_read_b128 v[168:171], v202 offset:32768
	s_waitcnt lgkmcnt(6)
	v_mfma_f32_16x16x32_bf16 v[88:91], v[176:179], v[104:107], v[88:91]
	v_add_f32_e32 v220, v220, v80
	v_add_f32_e32 v221, v221, v84
	v_mfma_f32_16x16x32_bf16 v[92:95], v[176:179], v[120:123], v[92:95]
	v_add_f32_e32 v220, v220, v81
	ds_read_b128 v[172:175], v209 offset:18432
	s_waitcnt lgkmcnt(6)
	v_mfma_f32_16x16x32_bf16 v[48:51], v[180:183], v[242:245], v[48:51]
	v_add_f32_e32 v221, v221, v85
	v_add_f32_e32 v220, v220, v82
	v_mfma_f32_16x16x32_bf16 v[52:55], v[180:183], v[204:207], v[52:55]
	v_add_f32_e32 v221, v221, v86
	ds_read_b128 v[176:179], v203 offset:32768
	s_waitcnt lgkmcnt(6)
	v_mfma_f32_16x16x32_bf16 v[92:95], v[230:233], v[124:127], v[92:95]
	v_add_f32_e32 v220, v220, v83
	v_add_f32_e32 v221, v221, v87
	v_mfma_f32_16x16x32_bf16 v[88:91], v[230:233], v[108:111], v[88:91]
	v_cvt_pk_bf16_f32 v218, v72, v73
	ds_read_b128 v[180:183], v209 offset:20480
	s_waitcnt lgkmcnt(6)
	v_mfma_f32_16x16x32_bf16 v[60:63], v[234:237], v[204:207], v[60:63]
	v_cvt_pk_bf16_f32 v219, v74, v75
	v_cvt_pk_bf16_f32 v240, v76, v77
	v_mfma_f32_16x16x32_bf16 v[56:59], v[234:237], v[242:245], v[56:59]
	v_cvt_pk_bf16_f32 v241, v78, v79
	ds_read_b128 v[230:233], v246 offset:32768
	s_waitcnt lgkmcnt(6)
	v_mfma_f32_16x16x32_bf16 v[64:67], v[160:163], v[96:99], 0
	v_exp_f32_e32 v88, v88
	v_mfma_f32_16x16x32_bf16 v[68:71], v[160:163], v[112:115], 0
	v_exp_f32_e32 v92, v92
	ds_read_b128 v[234:237], v209 offset:22528
	s_add_u32 s8, s16, 0x3bc00280
	s_addc_u32 s9, s17, 0
	s_add_u32 s6, s15, 0x23a60000
	s_addc_u32 s7, s14, 0
	s_waitcnt lgkmcnt(6)
	v_mfma_f32_16x16x32_bf16 v[0:3], v[164:167], v[216:219], v[0:3]
	v_cvt_pk_bf16_f32 v242, v80, v81
	v_mfma_f32_16x16x32_bf16 v[4:7], v[164:167], v[238:241], v[4:7]
	v_exp_f32_e32 v89, v89
	ds_read_b128 v[160:163], v201 offset:36864
	s_waitcnt vmcnt(4)
	ds_write_b128 v225, v[136:139] offset:0
	s_waitcnt lgkmcnt(7)
	v_mfma_f32_16x16x32_bf16 v[68:71], v[168:171], v[116:119], v[68:71]
	v_exp_f32_e32 v93, v93
	v_mfma_f32_16x16x32_bf16 v[64:67], v[168:171], v[100:103], v[64:67]
	v_cvt_pk_bf16_f32 v243, v82, v83
	ds_read_b128 v[164:167], v209 offset:24576
	ds_write_b128 v226, v[140:143] offset:0
	s_waitcnt lgkmcnt(8)
	v_mfma_f32_16x16x32_bf16 v[12:15], v[172:175], v[238:241], v[12:15]
	v_exp_f32_e32 v90, v90
	v_mfma_f32_16x16x32_bf16 v[8:11], v[172:175], v[216:219], v[8:11]
	v_exp_f32_e32 v94, v94
	ds_read_b128 v[168:171], v202 offset:36864
	ds_write_b64 v227, v[148:149] offset:49152
	s_waitcnt lgkmcnt(9)
	v_mfma_f32_16x16x32_bf16 v[64:67], v[176:179], v[104:107], v[64:67]
	v_cvt_pk_bf16_f32 v204, v84, v85
	v_mfma_f32_16x16x32_bf16 v[68:71], v[176:179], v[120:123], v[68:71]
	v_exp_f32_e32 v91, v91
	ds_read_b128 v[172:175], v209 offset:26624
	ds_write_b64 v228, v[150:151] offset:49152
	s_waitcnt lgkmcnt(10)
	v_mfma_f32_16x16x32_bf16 v[16:19], v[180:183], v[216:219], v[16:19]
	v_exp_f32_e32 v95, v95
	v_mfma_f32_16x16x32_bf16 v[20:23], v[180:183], v[238:241], v[20:23]
	v_cvt_pk_bf16_f32 v205, v86, v87
	v_add_f32_e32 v220, v220, v88
	ds_read_b128 v[176:179], v203 offset:36864
	ds_write_b64 v229, v[144:145] offset:49152
	s_waitcnt lgkmcnt(11)
	v_mfma_f32_16x16x32_bf16 v[68:71], v[230:233], v[124:127], v[68:71]
	v_add_f32_e32 v221, v221, v92
	v_add_f32_e32 v220, v220, v89
	v_mfma_f32_16x16x32_bf16 v[64:67], v[230:233], v[108:111], v[64:67]
	v_add_f32_e32 v221, v221, v93
	v_cvt_pk_bf16_f32 v244, v88, v89
	ds_read_b128 v[180:183], v209 offset:28672
	ds_write_b64 v184, v[146:147] offset:49152
	s_waitcnt lgkmcnt(12)
	v_mfma_f32_16x16x32_bf16 v[28:31], v[234:237], v[238:241], v[28:31]
	v_cvt_pk_bf16_f32 v245, v90, v91
	v_cvt_pk_bf16_f32 v206, v92, v93
	v_mfma_f32_16x16x32_bf16 v[24:27], v[234:237], v[216:219], v[24:27]
	v_cvt_pk_bf16_f32 v207, v94, v95
	ds_read_b128 v[230:233], v246 offset:36864
	global_load_dwordx4 v[148:151], v198, s[8:9]
	s_waitcnt lgkmcnt(12)
	v_mfma_f32_16x16x32_bf16 v[72:75], v[160:163], v[96:99], 0
	v_add_f32_e32 v220, v220, v90
	v_add_f32_e32 v221, v221, v94
	v_mfma_f32_16x16x32_bf16 v[76:79], v[160:163], v[112:115], 0
	v_add_f32_e32 v220, v220, v91
	v_add_f32_e32 v221, v221, v95
	ds_read_b128 v[234:237], v209 offset:30720
	global_load_dwordx4 v[144:147], v199, s[8:9]
	s_waitcnt lgkmcnt(11)
	v_mfma_f32_16x16x32_bf16 v[32:35], v[164:167], v[216:219], v[32:35]
	v_add_f32_e32 v194, v194, v220
	v_add_f32_e32 v195, v195, v221
	v_mfma_f32_16x16x32_bf16 v[36:39], v[164:167], v[238:241], v[36:39]
	v_exp_f32_e32 v64, v64
	ds_read_b128 v[160:163], v201 offset:40960
	global_load_dwordx4 v[136:139], v196, s[6:7]
	s_waitcnt lgkmcnt(10)
	v_mfma_f32_16x16x32_bf16 v[76:79], v[168:171], v[116:119], v[76:79]
	v_exp_f32_e32 v68, v68
	v_mfma_f32_16x16x32_bf16 v[72:75], v[168:171], v[100:103], v[72:75]
	v_exp_f32_e32 v65, v65
	ds_read_b128 v[164:167], v210 offset:16384
	global_load_dwordx4 v[140:143], v197, s[6:7]
	s_waitcnt lgkmcnt(9)
	v_mfma_f32_16x16x32_bf16 v[44:47], v[172:175], v[238:241], v[44:47]
	v_exp_f32_e32 v69, v69
	v_mfma_f32_16x16x32_bf16 v[40:43], v[172:175], v[216:219], v[40:43]
	v_exp_f32_e32 v66, v66
	ds_read_b128 v[168:171], v202 offset:40960
	s_waitcnt lgkmcnt(8)
	v_mfma_f32_16x16x32_bf16 v[72:75], v[176:179], v[104:107], v[72:75]
	v_exp_f32_e32 v70, v70
	v_mfma_f32_16x16x32_bf16 v[76:79], v[176:179], v[120:123], v[76:79]
	v_exp_f32_e32 v67, v67
	ds_read_b128 v[172:175], v210 offset:18432
	s_waitcnt lgkmcnt(7)
	v_mfma_f32_16x16x32_bf16 v[48:51], v[180:183], v[216:219], v[48:51]
	v_exp_f32_e32 v71, v71
	v_mfma_f32_16x16x32_bf16 v[52:55], v[180:183], v[238:241], v[52:55]
	v_add_f32_e32 v220, v64, v65
	ds_read_b128 v[176:179], v203 offset:40960
	s_waitcnt lgkmcnt(6)
	v_mfma_f32_16x16x32_bf16 v[76:79], v[230:233], v[124:127], v[76:79]
	v_add_f32_e32 v221, v68, v69
	v_mfma_f32_16x16x32_bf16 v[72:75], v[230:233], v[108:111], v[72:75]
	v_add_f32_e32 v220, v220, v66
	ds_read_b128 v[180:183], v210 offset:20480
	s_waitcnt lgkmcnt(6)
	v_mfma_f32_16x16x32_bf16 v[60:63], v[234:237], v[238:241], v[60:63]
	v_add_f32_e32 v221, v221, v70
	v_add_f32_e32 v220, v220, v67
	v_mfma_f32_16x16x32_bf16 v[56:59], v[234:237], v[216:219], v[56:59]
	v_add_f32_e32 v221, v221, v71
	ds_read_b128 v[230:233], v246 offset:40960
	s_waitcnt lgkmcnt(6)
	v_mfma_f32_16x16x32_bf16 v[80:83], v[160:163], v[96:99], 0
	v_exp_f32_e32 v72, v72
	v_mfma_f32_16x16x32_bf16 v[84:87], v[160:163], v[112:115], 0
	v_exp_f32_e32 v76, v76
	ds_read_b128 v[234:237], v210 offset:22528
	s_waitcnt lgkmcnt(6)
	v_mfma_f32_16x16x32_bf16 v[0:3], v[164:167], v[242:245], v[0:3]
	v_exp_f32_e32 v73, v73
	v_mfma_f32_16x16x32_bf16 v[4:7], v[164:167], v[204:207], v[4:7]
	v_exp_f32_e32 v77, v77
	ds_read_b128 v[160:163], v201 offset:45056
	s_waitcnt lgkmcnt(6)
	v_mfma_f32_16x16x32_bf16 v[84:87], v[168:171], v[116:119], v[84:87]
	v_exp_f32_e32 v74, v74
	v_mfma_f32_16x16x32_bf16 v[80:83], v[168:171], v[100:103], v[80:83]
	v_exp_f32_e32 v78, v78
	ds_read_b128 v[164:167], v210 offset:24576
	s_waitcnt lgkmcnt(6)
	v_mfma_f32_16x16x32_bf16 v[12:15], v[172:175], v[204:207], v[12:15]
	v_exp_f32_e32 v75, v75
	v_mfma_f32_16x16x32_bf16 v[8:11], v[172:175], v[242:245], v[8:11]
	v_exp_f32_e32 v79, v79
	ds_read_b128 v[168:171], v202 offset:45056
	s_waitcnt lgkmcnt(6)
	v_mfma_f32_16x16x32_bf16 v[80:83], v[176:179], v[104:107], v[80:83]
	v_add_f32_e32 v220, v220, v72
	v_add_f32_e32 v221, v221, v76
	v_mfma_f32_16x16x32_bf16 v[84:87], v[176:179], v[120:123], v[84:87]
	v_add_f32_e32 v220, v220, v73
	ds_read_b128 v[172:175], v210 offset:26624
	s_waitcnt lgkmcnt(6)
	v_mfma_f32_16x16x32_bf16 v[16:19], v[180:183], v[242:245], v[16:19]
	v_add_f32_e32 v221, v221, v77
	v_add_f32_e32 v220, v220, v74
	v_mfma_f32_16x16x32_bf16 v[20:23], v[180:183], v[204:207], v[20:23]
	v_add_f32_e32 v221, v221, v78
	ds_read_b128 v[176:179], v203 offset:45056
	s_waitcnt lgkmcnt(6)
	v_mfma_f32_16x16x32_bf16 v[84:87], v[230:233], v[124:127], v[84:87]
	v_add_f32_e32 v220, v220, v75
	v_add_f32_e32 v221, v221, v79
	v_mfma_f32_16x16x32_bf16 v[80:83], v[230:233], v[108:111], v[80:83]
	v_cvt_pk_bf16_f32 v216, v64, v65
	ds_read_b128 v[180:183], v210 offset:28672
	s_waitcnt lgkmcnt(6)
	v_mfma_f32_16x16x32_bf16 v[28:31], v[234:237], v[204:207], v[28:31]
	v_cvt_pk_bf16_f32 v217, v66, v67
	v_cvt_pk_bf16_f32 v238, v68, v69
	v_mfma_f32_16x16x32_bf16 v[24:27], v[234:237], v[242:245], v[24:27]
	v_cvt_pk_bf16_f32 v239, v70, v71
	ds_read_b128 v[230:233], v246 offset:45056
	s_waitcnt lgkmcnt(6)
	v_mfma_f32_16x16x32_bf16 v[88:91], v[160:163], v[96:99], 0
	v_exp_f32_e32 v80, v80
	v_mfma_f32_16x16x32_bf16 v[92:95], v[160:163], v[112:115], 0
	v_exp_f32_e32 v84, v84
	ds_read_b128 v[234:237], v210 offset:30720
	s_waitcnt lgkmcnt(6)
	v_mfma_f32_16x16x32_bf16 v[32:35], v[164:167], v[242:245], v[32:35]
	v_exp_f32_e32 v81, v81
	v_mfma_f32_16x16x32_bf16 v[36:39], v[164:167], v[204:207], v[36:39]
	v_exp_f32_e32 v85, v85
	s_waitcnt lgkmcnt(5)
	v_mfma_f32_16x16x32_bf16 v[92:95], v[168:171], v[116:119], v[92:95]
	v_exp_f32_e32 v82, v82
	v_mfma_f32_16x16x32_bf16 v[88:91], v[168:171], v[100:103], v[88:91]
	v_exp_f32_e32 v86, v86
	s_waitcnt lgkmcnt(4)
	v_mfma_f32_16x16x32_bf16 v[44:47], v[172:175], v[204:207], v[44:47]
	v_exp_f32_e32 v83, v83
	v_mfma_f32_16x16x32_bf16 v[40:43], v[172:175], v[242:245], v[40:43]
	v_exp_f32_e32 v87, v87
	s_waitcnt lgkmcnt(3)
	v_mfma_f32_16x16x32_bf16 v[88:91], v[176:179], v[104:107], v[88:91]
	v_add_f32_e32 v220, v220, v80
	v_add_f32_e32 v221, v221, v84
	v_mfma_f32_16x16x32_bf16 v[92:95], v[176:179], v[120:123], v[92:95]
	v_add_f32_e32 v220, v220, v81
	s_waitcnt lgkmcnt(2)
	v_mfma_f32_16x16x32_bf16 v[48:51], v[180:183], v[242:245], v[48:51]
	v_add_f32_e32 v221, v221, v85
	v_add_f32_e32 v220, v220, v82
	v_mfma_f32_16x16x32_bf16 v[52:55], v[180:183], v[204:207], v[52:55]
	v_add_f32_e32 v221, v221, v86
	s_waitcnt lgkmcnt(1)
	v_mfma_f32_16x16x32_bf16 v[92:95], v[230:233], v[124:127], v[92:95]
	v_add_f32_e32 v220, v220, v83
	v_add_f32_e32 v221, v221, v87
	v_mfma_f32_16x16x32_bf16 v[88:91], v[230:233], v[108:111], v[88:91]
	v_cvt_pk_bf16_f32 v218, v72, v73
	s_waitcnt lgkmcnt(0)
	v_mfma_f32_16x16x32_bf16 v[60:63], v[234:237], v[204:207], v[60:63]
	v_cvt_pk_bf16_f32 v219, v74, v75
	v_cvt_pk_bf16_f32 v240, v76, v77
	v_mfma_f32_16x16x32_bf16 v[56:59], v[234:237], v[242:245], v[56:59]
	v_cvt_pk_bf16_f32 v241, v78, v79
	s_waitcnt lgkmcnt(0)
	s_barrier
	ds_read_b128 v[160:163], v201 offset:49152
	ds_read_b128 v[164:167], v209 offset:32768
	ds_read_b128 v[168:171], v202 offset:49152
	ds_read_b128 v[172:175], v209 offset:34816
	ds_read_b128 v[176:179], v203 offset:49152
	ds_read_b128 v[180:183], v209 offset:36864
	ds_read_b128 v[230:233], v246 offset:49152
	s_waitcnt lgkmcnt(6)
	v_mfma_f32_16x16x32_bf16 v[64:67], v[160:163], v[96:99], 0
	v_exp_f32_e32 v88, v88
	v_mfma_f32_16x16x32_bf16 v[68:71], v[160:163], v[112:115], 0
	v_exp_f32_e32 v92, v92
	ds_read_b128 v[234:237], v209 offset:38912
	s_add_u32 s8, s16, 0x3bc00300
	s_addc_u32 s9, s17, 0
	s_add_u32 s6, s15, 0x23a70000
	s_addc_u32 s7, s14, 0
	s_waitcnt lgkmcnt(6)
	v_mfma_f32_16x16x32_bf16 v[0:3], v[164:167], v[216:219], v[0:3]
	v_cvt_pk_bf16_f32 v242, v80, v81
	v_mfma_f32_16x16x32_bf16 v[4:7], v[164:167], v[238:241], v[4:7]
	v_exp_f32_e32 v89, v89
	ds_read_b128 v[160:163], v201 offset:53248
	s_waitcnt vmcnt(4)
	ds_write_b128 v225, v[152:155] offset:16384
	s_waitcnt lgkmcnt(7)
	v_mfma_f32_16x16x32_bf16 v[68:71], v[168:171], v[116:119], v[68:71]
	v_exp_f32_e32 v93, v93
	v_mfma_f32_16x16x32_bf16 v[64:67], v[168:171], v[100:103], v[64:67]
	v_cvt_pk_bf16_f32 v243, v82, v83
	ds_read_b128 v[164:167], v209 offset:40960
	ds_write_b128 v226, v[156:159] offset:16384
	s_waitcnt lgkmcnt(8)
	v_mfma_f32_16x16x32_bf16 v[12:15], v[172:175], v[238:241], v[12:15]
	v_exp_f32_e32 v90, v90
	v_mfma_f32_16x16x32_bf16 v[8:11], v[172:175], v[216:219], v[8:11]
	v_exp_f32_e32 v94, v94
	ds_read_b128 v[168:171], v202 offset:53248
	ds_write_b64 v227, v[132:133] offset:0
	s_waitcnt lgkmcnt(9)
	v_mfma_f32_16x16x32_bf16 v[64:67], v[176:179], v[104:107], v[64:67]
	v_cvt_pk_bf16_f32 v204, v84, v85
	v_mfma_f32_16x16x32_bf16 v[68:71], v[176:179], v[120:123], v[68:71]
	v_exp_f32_e32 v91, v91
	ds_read_b128 v[172:175], v209 offset:43008
	ds_write_b64 v228, v[134:135] offset:0
	s_waitcnt lgkmcnt(10)
	v_mfma_f32_16x16x32_bf16 v[16:19], v[180:183], v[216:219], v[16:19]
	v_exp_f32_e32 v95, v95
	v_mfma_f32_16x16x32_bf16 v[20:23], v[180:183], v[238:241], v[20:23]
	v_cvt_pk_bf16_f32 v205, v86, v87
	v_add_f32_e32 v220, v220, v88
	ds_read_b128 v[176:179], v203 offset:53248
	ds_write_b64 v229, v[128:129] offset:0
	s_waitcnt lgkmcnt(11)
	v_mfma_f32_16x16x32_bf16 v[68:71], v[230:233], v[124:127], v[68:71]
	v_add_f32_e32 v221, v221, v92
	v_add_f32_e32 v220, v220, v89
	v_mfma_f32_16x16x32_bf16 v[64:67], v[230:233], v[108:111], v[64:67]
	v_add_f32_e32 v221, v221, v93
	v_cvt_pk_bf16_f32 v244, v88, v89
	ds_read_b128 v[180:183], v209 offset:45056
	ds_write_b64 v184, v[130:131] offset:0
	s_waitcnt lgkmcnt(12)
	v_mfma_f32_16x16x32_bf16 v[28:31], v[234:237], v[238:241], v[28:31]
	v_cvt_pk_bf16_f32 v245, v90, v91
	v_cvt_pk_bf16_f32 v206, v92, v93
	v_mfma_f32_16x16x32_bf16 v[24:27], v[234:237], v[216:219], v[24:27]
	v_cvt_pk_bf16_f32 v207, v94, v95
	ds_read_b128 v[230:233], v246 offset:53248
	global_load_dwordx4 v[132:135], v198, s[8:9]
	s_waitcnt lgkmcnt(12)
	v_mfma_f32_16x16x32_bf16 v[72:75], v[160:163], v[96:99], 0
	v_add_f32_e32 v220, v220, v90
	v_add_f32_e32 v221, v221, v94
	v_mfma_f32_16x16x32_bf16 v[76:79], v[160:163], v[112:115], 0
	v_add_f32_e32 v220, v220, v91
	v_add_f32_e32 v221, v221, v95
	ds_read_b128 v[234:237], v209 offset:47104
	global_load_dwordx4 v[128:131], v199, s[8:9]
	s_waitcnt lgkmcnt(11)
	v_mfma_f32_16x16x32_bf16 v[32:35], v[164:167], v[216:219], v[32:35]
	v_add_f32_e32 v194, v194, v220
	v_add_f32_e32 v195, v195, v221
	v_mfma_f32_16x16x32_bf16 v[36:39], v[164:167], v[238:241], v[36:39]
	v_exp_f32_e32 v64, v64
	ds_read_b128 v[160:163], v201 offset:57344
	global_load_dwordx4 v[152:155], v196, s[6:7]
	s_waitcnt lgkmcnt(10)
	v_mfma_f32_16x16x32_bf16 v[76:79], v[168:171], v[116:119], v[76:79]
	v_exp_f32_e32 v68, v68
	v_mfma_f32_16x16x32_bf16 v[72:75], v[168:171], v[100:103], v[72:75]
	v_exp_f32_e32 v65, v65
	ds_read_b128 v[164:167], v210 offset:32768
	global_load_dwordx4 v[156:159], v197, s[6:7]
	s_waitcnt lgkmcnt(9)
	v_mfma_f32_16x16x32_bf16 v[44:47], v[172:175], v[238:241], v[44:47]
	v_exp_f32_e32 v69, v69
	v_mfma_f32_16x16x32_bf16 v[40:43], v[172:175], v[216:219], v[40:43]
	v_exp_f32_e32 v66, v66
	ds_read_b128 v[168:171], v202 offset:57344
	s_waitcnt lgkmcnt(8)
	v_mfma_f32_16x16x32_bf16 v[72:75], v[176:179], v[104:107], v[72:75]
	v_exp_f32_e32 v70, v70
	v_mfma_f32_16x16x32_bf16 v[76:79], v[176:179], v[120:123], v[76:79]
	v_exp_f32_e32 v67, v67
	ds_read_b128 v[172:175], v210 offset:34816
	s_waitcnt lgkmcnt(7)
	v_mfma_f32_16x16x32_bf16 v[48:51], v[180:183], v[216:219], v[48:51]
	v_exp_f32_e32 v71, v71
	v_mfma_f32_16x16x32_bf16 v[52:55], v[180:183], v[238:241], v[52:55]
	v_add_f32_e32 v220, v64, v65
	ds_read_b128 v[176:179], v203 offset:57344
	s_waitcnt lgkmcnt(6)
	v_mfma_f32_16x16x32_bf16 v[76:79], v[230:233], v[124:127], v[76:79]
	v_add_f32_e32 v221, v68, v69
	v_mfma_f32_16x16x32_bf16 v[72:75], v[230:233], v[108:111], v[72:75]
	v_add_f32_e32 v220, v220, v66
	ds_read_b128 v[180:183], v210 offset:36864
	s_waitcnt lgkmcnt(6)
	v_mfma_f32_16x16x32_bf16 v[60:63], v[234:237], v[238:241], v[60:63]
	v_add_f32_e32 v221, v221, v70
	v_add_f32_e32 v220, v220, v67
	v_mfma_f32_16x16x32_bf16 v[56:59], v[234:237], v[216:219], v[56:59]
	v_add_f32_e32 v221, v221, v71
	ds_read_b128 v[230:233], v246 offset:57344
	s_waitcnt lgkmcnt(6)
	v_mfma_f32_16x16x32_bf16 v[80:83], v[160:163], v[96:99], 0
	v_exp_f32_e32 v72, v72
	v_mfma_f32_16x16x32_bf16 v[84:87], v[160:163], v[112:115], 0
	v_exp_f32_e32 v76, v76
	ds_read_b128 v[234:237], v210 offset:38912
	s_waitcnt lgkmcnt(6)
	v_mfma_f32_16x16x32_bf16 v[0:3], v[164:167], v[242:245], v[0:3]
	v_exp_f32_e32 v73, v73
	v_mfma_f32_16x16x32_bf16 v[4:7], v[164:167], v[204:207], v[4:7]
	v_exp_f32_e32 v77, v77
	ds_read_b128 v[160:163], v201 offset:61440
	s_waitcnt lgkmcnt(6)
	v_mfma_f32_16x16x32_bf16 v[84:87], v[168:171], v[116:119], v[84:87]
	v_exp_f32_e32 v74, v74
	v_mfma_f32_16x16x32_bf16 v[80:83], v[168:171], v[100:103], v[80:83]
	v_exp_f32_e32 v78, v78
	ds_read_b128 v[164:167], v210 offset:40960
	s_waitcnt lgkmcnt(6)
	v_mfma_f32_16x16x32_bf16 v[12:15], v[172:175], v[204:207], v[12:15]
	v_exp_f32_e32 v75, v75
	v_mfma_f32_16x16x32_bf16 v[8:11], v[172:175], v[242:245], v[8:11]
	v_exp_f32_e32 v79, v79
	ds_read_b128 v[168:171], v202 offset:61440
	s_waitcnt lgkmcnt(6)
	v_mfma_f32_16x16x32_bf16 v[80:83], v[176:179], v[104:107], v[80:83]
	v_add_f32_e32 v220, v220, v72
	v_add_f32_e32 v221, v221, v76
	v_mfma_f32_16x16x32_bf16 v[84:87], v[176:179], v[120:123], v[84:87]
	v_add_f32_e32 v220, v220, v73
	ds_read_b128 v[172:175], v210 offset:43008
	s_waitcnt lgkmcnt(6)
	v_mfma_f32_16x16x32_bf16 v[16:19], v[180:183], v[242:245], v[16:19]
	v_add_f32_e32 v221, v221, v77
	v_add_f32_e32 v220, v220, v74
	v_mfma_f32_16x16x32_bf16 v[20:23], v[180:183], v[204:207], v[20:23]
	v_add_f32_e32 v221, v221, v78
	ds_read_b128 v[176:179], v203 offset:61440
	s_waitcnt lgkmcnt(6)
	v_mfma_f32_16x16x32_bf16 v[84:87], v[230:233], v[124:127], v[84:87]
	v_add_f32_e32 v220, v220, v75
	v_add_f32_e32 v221, v221, v79
	v_mfma_f32_16x16x32_bf16 v[80:83], v[230:233], v[108:111], v[80:83]
	v_cvt_pk_bf16_f32 v216, v64, v65
	ds_read_b128 v[180:183], v210 offset:45056
	s_waitcnt lgkmcnt(6)
	v_mfma_f32_16x16x32_bf16 v[28:31], v[234:237], v[204:207], v[28:31]
	v_cvt_pk_bf16_f32 v217, v66, v67
	v_cvt_pk_bf16_f32 v238, v68, v69
	v_mfma_f32_16x16x32_bf16 v[24:27], v[234:237], v[242:245], v[24:27]
	v_cvt_pk_bf16_f32 v239, v70, v71
	ds_read_b128 v[230:233], v246 offset:61440
	s_waitcnt lgkmcnt(6)
	v_mfma_f32_16x16x32_bf16 v[88:91], v[160:163], v[96:99], 0
	v_exp_f32_e32 v80, v80
	v_mfma_f32_16x16x32_bf16 v[92:95], v[160:163], v[112:115], 0
	v_exp_f32_e32 v84, v84
	ds_read_b128 v[234:237], v210 offset:47104
	s_waitcnt lgkmcnt(6)
	v_mfma_f32_16x16x32_bf16 v[32:35], v[164:167], v[242:245], v[32:35]
	v_exp_f32_e32 v81, v81
	v_mfma_f32_16x16x32_bf16 v[36:39], v[164:167], v[204:207], v[36:39]
	v_exp_f32_e32 v85, v85
	ds_read_b128 v[160:163], v201 offset:0
	s_waitcnt lgkmcnt(6)
	v_mfma_f32_16x16x32_bf16 v[92:95], v[168:171], v[116:119], v[92:95]
	v_exp_f32_e32 v82, v82
	v_mfma_f32_16x16x32_bf16 v[88:91], v[168:171], v[100:103], v[88:91]
	v_exp_f32_e32 v86, v86
	ds_read_b128 v[164:167], v209 offset:49152
	s_waitcnt lgkmcnt(6)
	v_mfma_f32_16x16x32_bf16 v[44:47], v[172:175], v[204:207], v[44:47]
	v_exp_f32_e32 v83, v83
	v_mfma_f32_16x16x32_bf16 v[40:43], v[172:175], v[242:245], v[40:43]
	v_exp_f32_e32 v87, v87
	ds_read_b128 v[168:171], v202 offset:0
	s_waitcnt lgkmcnt(6)
	v_mfma_f32_16x16x32_bf16 v[88:91], v[176:179], v[104:107], v[88:91]
	v_add_f32_e32 v220, v220, v80
	v_add_f32_e32 v221, v221, v84
	v_mfma_f32_16x16x32_bf16 v[92:95], v[176:179], v[120:123], v[92:95]
	v_add_f32_e32 v220, v220, v81
	ds_read_b128 v[172:175], v209 offset:51200
	s_waitcnt lgkmcnt(6)
	v_mfma_f32_16x16x32_bf16 v[48:51], v[180:183], v[242:245], v[48:51]
	v_add_f32_e32 v221, v221, v85
	v_add_f32_e32 v220, v220, v82
	v_mfma_f32_16x16x32_bf16 v[52:55], v[180:183], v[204:207], v[52:55]
	v_add_f32_e32 v221, v221, v86
	ds_read_b128 v[176:179], v203 offset:0
	s_waitcnt lgkmcnt(6)
	v_mfma_f32_16x16x32_bf16 v[92:95], v[230:233], v[124:127], v[92:95]
	v_add_f32_e32 v220, v220, v83
	v_add_f32_e32 v221, v221, v87
	v_mfma_f32_16x16x32_bf16 v[88:91], v[230:233], v[108:111], v[88:91]
	v_cvt_pk_bf16_f32 v218, v72, v73
	ds_read_b128 v[180:183], v209 offset:53248
	s_waitcnt lgkmcnt(6)
	v_mfma_f32_16x16x32_bf16 v[60:63], v[234:237], v[204:207], v[60:63]
	v_cvt_pk_bf16_f32 v219, v74, v75
	v_cvt_pk_bf16_f32 v240, v76, v77
	v_mfma_f32_16x16x32_bf16 v[56:59], v[234:237], v[242:245], v[56:59]
	v_cvt_pk_bf16_f32 v241, v78, v79
	ds_read_b128 v[230:233], v246 offset:0
	s_waitcnt lgkmcnt(6)
	v_mfma_f32_16x16x32_bf16 v[64:67], v[160:163], v[96:99], 0
	v_exp_f32_e32 v88, v88
	v_mfma_f32_16x16x32_bf16 v[68:71], v[160:163], v[112:115], 0
	v_exp_f32_e32 v92, v92
	ds_read_b128 v[234:237], v209 offset:55296
	s_add_u32 s8, s16, 0x3bc00380
	s_addc_u32 s9, s17, 0
	s_add_u32 s6, s15, 0x23a80000
	s_addc_u32 s7, s14, 0
	s_waitcnt lgkmcnt(6)
	v_mfma_f32_16x16x32_bf16 v[0:3], v[164:167], v[216:219], v[0:3]
	v_cvt_pk_bf16_f32 v242, v80, v81
	v_mfma_f32_16x16x32_bf16 v[4:7], v[164:167], v[238:241], v[4:7]
	v_exp_f32_e32 v89, v89
	ds_read_b128 v[160:163], v201 offset:4096
	s_waitcnt vmcnt(4)
	ds_write_b128 v225, v[136:139] offset:32768
	s_waitcnt lgkmcnt(7)
	v_mfma_f32_16x16x32_bf16 v[68:71], v[168:171], v[116:119], v[68:71]
	v_exp_f32_e32 v93, v93
	v_mfma_f32_16x16x32_bf16 v[64:67], v[168:171], v[100:103], v[64:67]
	v_cvt_pk_bf16_f32 v243, v82, v83
	ds_read_b128 v[164:167], v209 offset:57344
	ds_write_b128 v226, v[140:143] offset:32768
	s_waitcnt lgkmcnt(8)
	v_mfma_f32_16x16x32_bf16 v[12:15], v[172:175], v[238:241], v[12:15]
	v_exp_f32_e32 v90, v90
	v_mfma_f32_16x16x32_bf16 v[8:11], v[172:175], v[216:219], v[8:11]
	v_exp_f32_e32 v94, v94
	ds_read_b128 v[168:171], v202 offset:4096
	ds_write_b64 v227, v[148:149] offset:16384
	s_waitcnt lgkmcnt(9)
	v_mfma_f32_16x16x32_bf16 v[64:67], v[176:179], v[104:107], v[64:67]
	v_cvt_pk_bf16_f32 v204, v84, v85
	v_mfma_f32_16x16x32_bf16 v[68:71], v[176:179], v[120:123], v[68:71]
	v_exp_f32_e32 v91, v91
	ds_read_b128 v[172:175], v209 offset:59392
	ds_write_b64 v228, v[150:151] offset:16384
	s_waitcnt lgkmcnt(10)
	v_mfma_f32_16x16x32_bf16 v[16:19], v[180:183], v[216:219], v[16:19]
	v_exp_f32_e32 v95, v95
	v_mfma_f32_16x16x32_bf16 v[20:23], v[180:183], v[238:241], v[20:23]
	v_cvt_pk_bf16_f32 v205, v86, v87
	v_add_f32_e32 v220, v220, v88
	ds_read_b128 v[176:179], v203 offset:4096
	ds_write_b64 v229, v[144:145] offset:16384
	s_waitcnt lgkmcnt(11)
	v_mfma_f32_16x16x32_bf16 v[68:71], v[230:233], v[124:127], v[68:71]
	v_add_f32_e32 v221, v221, v92
	v_add_f32_e32 v220, v220, v89
	v_mfma_f32_16x16x32_bf16 v[64:67], v[230:233], v[108:111], v[64:67]
	v_add_f32_e32 v221, v221, v93
	v_cvt_pk_bf16_f32 v244, v88, v89
	ds_read_b128 v[180:183], v209 offset:61440
	ds_write_b64 v184, v[146:147] offset:16384
	s_waitcnt lgkmcnt(12)
	v_mfma_f32_16x16x32_bf16 v[28:31], v[234:237], v[238:241], v[28:31]
	v_cvt_pk_bf16_f32 v245, v90, v91
	v_cvt_pk_bf16_f32 v206, v92, v93
	v_mfma_f32_16x16x32_bf16 v[24:27], v[234:237], v[216:219], v[24:27]
	v_cvt_pk_bf16_f32 v207, v94, v95
	ds_read_b128 v[230:233], v246 offset:4096
	global_load_dwordx4 v[148:151], v198, s[8:9]
	s_waitcnt lgkmcnt(12)
	v_mfma_f32_16x16x32_bf16 v[72:75], v[160:163], v[96:99], 0
	v_add_f32_e32 v220, v220, v90
	v_add_f32_e32 v221, v221, v94
	v_mfma_f32_16x16x32_bf16 v[76:79], v[160:163], v[112:115], 0
	v_add_f32_e32 v220, v220, v91
	v_add_f32_e32 v221, v221, v95
	ds_read_b128 v[234:237], v209 offset:63488
	global_load_dwordx4 v[144:147], v199, s[8:9]
	s_waitcnt lgkmcnt(11)
	v_mfma_f32_16x16x32_bf16 v[32:35], v[164:167], v[216:219], v[32:35]
	v_add_f32_e32 v194, v194, v220
	v_add_f32_e32 v195, v195, v221
	v_mfma_f32_16x16x32_bf16 v[36:39], v[164:167], v[238:241], v[36:39]
	v_exp_f32_e32 v64, v64
	ds_read_b128 v[160:163], v201 offset:8192
	global_load_dwordx4 v[136:139], v196, s[6:7]
	s_waitcnt lgkmcnt(10)
	v_mfma_f32_16x16x32_bf16 v[76:79], v[168:171], v[116:119], v[76:79]
	v_exp_f32_e32 v68, v68
	v_mfma_f32_16x16x32_bf16 v[72:75], v[168:171], v[100:103], v[72:75]
	v_exp_f32_e32 v65, v65
	ds_read_b128 v[164:167], v210 offset:49152
	global_load_dwordx4 v[140:143], v197, s[6:7]
	s_waitcnt lgkmcnt(9)
	v_mfma_f32_16x16x32_bf16 v[44:47], v[172:175], v[238:241], v[44:47]
	v_exp_f32_e32 v69, v69
	v_mfma_f32_16x16x32_bf16 v[40:43], v[172:175], v[216:219], v[40:43]
	v_exp_f32_e32 v66, v66
	ds_read_b128 v[168:171], v202 offset:8192
	s_waitcnt lgkmcnt(8)
	v_mfma_f32_16x16x32_bf16 v[72:75], v[176:179], v[104:107], v[72:75]
	v_exp_f32_e32 v70, v70
	v_mfma_f32_16x16x32_bf16 v[76:79], v[176:179], v[120:123], v[76:79]
	v_exp_f32_e32 v67, v67
	ds_read_b128 v[172:175], v210 offset:51200
	s_waitcnt lgkmcnt(7)
	v_mfma_f32_16x16x32_bf16 v[48:51], v[180:183], v[216:219], v[48:51]
	v_exp_f32_e32 v71, v71
	v_mfma_f32_16x16x32_bf16 v[52:55], v[180:183], v[238:241], v[52:55]
	v_add_f32_e32 v220, v64, v65
	ds_read_b128 v[176:179], v203 offset:8192
	s_waitcnt lgkmcnt(6)
	v_mfma_f32_16x16x32_bf16 v[76:79], v[230:233], v[124:127], v[76:79]
	v_add_f32_e32 v221, v68, v69
	v_mfma_f32_16x16x32_bf16 v[72:75], v[230:233], v[108:111], v[72:75]
	v_add_f32_e32 v220, v220, v66
	ds_read_b128 v[180:183], v210 offset:53248
	s_waitcnt lgkmcnt(6)
	v_mfma_f32_16x16x32_bf16 v[60:63], v[234:237], v[238:241], v[60:63]
	v_add_f32_e32 v221, v221, v70
	v_add_f32_e32 v220, v220, v67
	v_mfma_f32_16x16x32_bf16 v[56:59], v[234:237], v[216:219], v[56:59]
	v_add_f32_e32 v221, v221, v71
	ds_read_b128 v[230:233], v246 offset:8192
	s_waitcnt lgkmcnt(6)
	v_mfma_f32_16x16x32_bf16 v[80:83], v[160:163], v[96:99], 0
	v_exp_f32_e32 v72, v72
	v_mfma_f32_16x16x32_bf16 v[84:87], v[160:163], v[112:115], 0
	v_exp_f32_e32 v76, v76
	ds_read_b128 v[234:237], v210 offset:55296
	s_waitcnt lgkmcnt(6)
	v_mfma_f32_16x16x32_bf16 v[0:3], v[164:167], v[242:245], v[0:3]
	v_exp_f32_e32 v73, v73
	v_mfma_f32_16x16x32_bf16 v[4:7], v[164:167], v[204:207], v[4:7]
	v_exp_f32_e32 v77, v77
	ds_read_b128 v[160:163], v201 offset:12288
	s_waitcnt lgkmcnt(6)
	v_mfma_f32_16x16x32_bf16 v[84:87], v[168:171], v[116:119], v[84:87]
	v_exp_f32_e32 v74, v74
	v_mfma_f32_16x16x32_bf16 v[80:83], v[168:171], v[100:103], v[80:83]
	v_exp_f32_e32 v78, v78
	ds_read_b128 v[164:167], v210 offset:57344
	s_waitcnt lgkmcnt(6)
	v_mfma_f32_16x16x32_bf16 v[12:15], v[172:175], v[204:207], v[12:15]
	v_exp_f32_e32 v75, v75
	v_mfma_f32_16x16x32_bf16 v[8:11], v[172:175], v[242:245], v[8:11]
	v_exp_f32_e32 v79, v79
	ds_read_b128 v[168:171], v202 offset:12288
	s_waitcnt lgkmcnt(6)
	v_mfma_f32_16x16x32_bf16 v[80:83], v[176:179], v[104:107], v[80:83]
	v_add_f32_e32 v220, v220, v72
	v_add_f32_e32 v221, v221, v76
	v_mfma_f32_16x16x32_bf16 v[84:87], v[176:179], v[120:123], v[84:87]
	v_add_f32_e32 v220, v220, v73
	ds_read_b128 v[172:175], v210 offset:59392
	s_add_u32 s10, s10, 0x200
	s_addc_u32 s11, s11, 0
	s_add_u32 s12, s12, 0x40000
	s_addc_u32 s13, s13, 0
	s_add_i32 s4, s4, 4
	s_cmpk_lt_u32 s4, 0x104
	s_cselect_b64 s[6:7], -1, 0
	s_and_b64 s[6:7], s[0:1], s[6:7]
	s_and_b64 vcc, exec, s[6:7]
	s_waitcnt lgkmcnt(6)
	v_mfma_f32_16x16x32_bf16 v[16:19], v[180:183], v[242:245], v[16:19]
	v_add_f32_e32 v221, v221, v77
	v_add_f32_e32 v220, v220, v74
	v_mfma_f32_16x16x32_bf16 v[20:23], v[180:183], v[204:207], v[20:23]
	v_add_f32_e32 v221, v221, v78
	ds_read_b128 v[176:179], v203 offset:12288
	s_waitcnt lgkmcnt(6)
	v_mfma_f32_16x16x32_bf16 v[84:87], v[230:233], v[124:127], v[84:87]
	v_add_f32_e32 v220, v220, v75
	v_add_f32_e32 v221, v221, v79
	v_mfma_f32_16x16x32_bf16 v[80:83], v[230:233], v[108:111], v[80:83]
	v_cvt_pk_bf16_f32 v216, v64, v65
	ds_read_b128 v[180:183], v210 offset:61440
	s_waitcnt lgkmcnt(6)
	v_mfma_f32_16x16x32_bf16 v[28:31], v[234:237], v[204:207], v[28:31]
	v_cvt_pk_bf16_f32 v217, v66, v67
	v_cvt_pk_bf16_f32 v238, v68, v69
	v_mfma_f32_16x16x32_bf16 v[24:27], v[234:237], v[242:245], v[24:27]
	v_cvt_pk_bf16_f32 v239, v70, v71
	ds_read_b128 v[230:233], v246 offset:12288
	s_waitcnt lgkmcnt(6)
	v_mfma_f32_16x16x32_bf16 v[88:91], v[160:163], v[96:99], 0
	v_exp_f32_e32 v80, v80
	v_mfma_f32_16x16x32_bf16 v[92:95], v[160:163], v[112:115], 0
	v_exp_f32_e32 v84, v84
	ds_read_b128 v[234:237], v210 offset:63488
	s_waitcnt lgkmcnt(6)
	v_mfma_f32_16x16x32_bf16 v[32:35], v[164:167], v[242:245], v[32:35]
	v_exp_f32_e32 v81, v81
	v_mfma_f32_16x16x32_bf16 v[36:39], v[164:167], v[204:207], v[36:39]
	v_exp_f32_e32 v85, v85
	s_waitcnt lgkmcnt(5)
	v_mfma_f32_16x16x32_bf16 v[92:95], v[168:171], v[116:119], v[92:95]
	v_exp_f32_e32 v82, v82
	v_mfma_f32_16x16x32_bf16 v[88:91], v[168:171], v[100:103], v[88:91]
	v_exp_f32_e32 v86, v86
	s_waitcnt lgkmcnt(4)
	v_mfma_f32_16x16x32_bf16 v[44:47], v[172:175], v[204:207], v[44:47]
	v_exp_f32_e32 v83, v83
	v_mfma_f32_16x16x32_bf16 v[40:43], v[172:175], v[242:245], v[40:43]
	v_exp_f32_e32 v87, v87
	s_waitcnt lgkmcnt(3)
	v_mfma_f32_16x16x32_bf16 v[88:91], v[176:179], v[104:107], v[88:91]
	v_add_f32_e32 v220, v220, v80
	v_add_f32_e32 v221, v221, v84
	v_mfma_f32_16x16x32_bf16 v[92:95], v[176:179], v[120:123], v[92:95]
	v_add_f32_e32 v220, v220, v81
	s_waitcnt lgkmcnt(2)
	v_mfma_f32_16x16x32_bf16 v[48:51], v[180:183], v[242:245], v[48:51]
	v_add_f32_e32 v221, v221, v85
	v_add_f32_e32 v220, v220, v82
	v_mfma_f32_16x16x32_bf16 v[52:55], v[180:183], v[204:207], v[52:55]
	v_add_f32_e32 v221, v221, v86
	s_waitcnt lgkmcnt(1)
	v_mfma_f32_16x16x32_bf16 v[92:95], v[230:233], v[124:127], v[92:95]
	v_add_f32_e32 v220, v220, v83
	v_add_f32_e32 v221, v221, v87
	v_mfma_f32_16x16x32_bf16 v[88:91], v[230:233], v[108:111], v[88:91]
	v_cvt_pk_bf16_f32 v218, v72, v73
	s_waitcnt lgkmcnt(0)
	v_mfma_f32_16x16x32_bf16 v[60:63], v[234:237], v[204:207], v[60:63]
	v_cvt_pk_bf16_f32 v219, v74, v75
	v_cvt_pk_bf16_f32 v240, v76, v77
	v_mfma_f32_16x16x32_bf16 v[56:59], v[234:237], v[242:245], v[56:59]
	v_cvt_pk_bf16_f32 v241, v78, v79
	s_cbranch_vccnz .LBB0_734
	s_waitcnt vmcnt(0)
	s_nop 7
	s_nop 7
	ds_swizzle_b32 v64, v194 offset:swizzle(SWAP,16)
	s_waitcnt lgkmcnt(0)
	v_add_f32_e32 v194, v194, v64
	v_mov_b32_e32 v65, v194
	s_nop 1
	v_permlane32_swap_b32_e32 v194, v65
	v_add_f32_e32 v194, v194, v65
	s_nop 0
	v_rcp_f32_e32 v66, v194
	ds_swizzle_b32 v64, v195 offset:swizzle(SWAP,16)
	s_waitcnt lgkmcnt(0)
	v_add_f32_e32 v195, v195, v64
	v_mov_b32_e32 v65, v195
	s_nop 1
	v_permlane32_swap_b32_e32 v195, v65
	v_add_f32_e32 v195, v195, v65
	s_nop 0
	v_rcp_f32_e32 v67, v195
	v_readlane_b32 s100, v250, 8
	v_mbcnt_lo_u32_b32 v68, -1, 0
	v_mbcnt_hi_u32_b32 v68, -1, v68
	v_and_b32_e32 v69, 15, v68
	v_lshrrev_b32_e32 v70, 4, v68
	s_lshr_b32 s101, s100, 1
	v_add_u32_e32 v69, s101, v69
	v_lshlrev_b32_e32 v69, 12, v69
	v_and_b32_e32 v71, 1, v70
	v_lshlrev_b32_e32 v71, 5, v71
	v_and_b32_e32 v70, 2, v70
	v_lshl_add_u32 v71, v70, 3, v71
	v_add_u32_e32 v70, v69, v71
	v_add_u32_e32 v71, 0x10000, v70
	v_mul_f32_e32 v0, v0, v66
	v_mul_f32_e32 v1, v1, v66
	v_mul_f32_e32 v2, v2, v66
	v_mul_f32_e32 v3, v3, v66
	v_mul_f32_e32 v8, v8, v66
	v_mul_f32_e32 v9, v9, v66
	v_mul_f32_e32 v10, v10, v66
	v_mul_f32_e32 v11, v11, v66
	v_cvt_pk_bf16_f32 v72, v0, v1
	v_cvt_pk_bf16_f32 v73, v2, v3
	v_cvt_pk_bf16_f32 v74, v8, v9
	v_cvt_pk_bf16_f32 v75, v10, v11
	s_nop 1
	v_permlane16_swap_b32_e32 v72, v74
	v_permlane16_swap_b32_e32 v73, v75
	s_nop 1
	global_store_dwordx4 v70, v[72:75], s[58:59] offset:0
	v_mul_f32_e32 v16, v16, v66
	v_mul_f32_e32 v17, v17, v66
	v_mul_f32_e32 v18, v18, v66
	v_mul_f32_e32 v19, v19, v66
	v_mul_f32_e32 v24, v24, v66
	v_mul_f32_e32 v25, v25, v66
	v_mul_f32_e32 v26, v26, v66
	v_mul_f32_e32 v27, v27, v66
	v_cvt_pk_bf16_f32 v76, v16, v17
	v_cvt_pk_bf16_f32 v77, v18, v19
	v_cvt_pk_bf16_f32 v78, v24, v25
	v_cvt_pk_bf16_f32 v79, v26, v27
	s_nop 1
	v_permlane16_swap_b32_e32 v76, v78
	v_permlane16_swap_b32_e32 v77, v79
	s_nop 1
	global_store_dwordx4 v70, v[76:79], s[58:59] offset:64
	v_mul_f32_e32 v32, v32, v66
	v_mul_f32_e32 v33, v33, v66
	v_mul_f32_e32 v34, v34, v66
	v_mul_f32_e32 v35, v35, v66
	v_mul_f32_e32 v40, v40, v66
	v_mul_f32_e32 v41, v41, v66
	v_mul_f32_e32 v42, v42, v66
	v_mul_f32_e32 v43, v43, v66
	v_cvt_pk_bf16_f32 v80, v32, v33
	v_cvt_pk_bf16_f32 v81, v34, v35
	v_cvt_pk_bf16_f32 v82, v40, v41
	v_cvt_pk_bf16_f32 v83, v42, v43
	s_nop 1
	v_permlane16_swap_b32_e32 v80, v82
	v_permlane16_swap_b32_e32 v81, v83
	s_nop 1
	global_store_dwordx4 v70, v[80:83], s[58:59] offset:128
	v_mul_f32_e32 v48, v48, v66
	v_mul_f32_e32 v49, v49, v66
	v_mul_f32_e32 v50, v50, v66
	v_mul_f32_e32 v51, v51, v66
	v_mul_f32_e32 v56, v56, v66
	v_mul_f32_e32 v57, v57, v66
	v_mul_f32_e32 v58, v58, v66
	v_mul_f32_e32 v59, v59, v66
	v_cvt_pk_bf16_f32 v84, v48, v49
	v_cvt_pk_bf16_f32 v85, v50, v51
	v_cvt_pk_bf16_f32 v86, v56, v57
	v_cvt_pk_bf16_f32 v87, v58, v59
	s_nop 1
	v_permlane16_swap_b32_e32 v84, v86
	v_permlane16_swap_b32_e32 v85, v87
	s_nop 1
	global_store_dwordx4 v70, v[84:87], s[58:59] offset:192
	v_mul_f32_e32 v4, v4, v67
	v_mul_f32_e32 v5, v5, v67
	v_mul_f32_e32 v6, v6, v67
	v_mul_f32_e32 v7, v7, v67
	v_mul_f32_e32 v12, v12, v67
	v_mul_f32_e32 v13, v13, v67
	v_mul_f32_e32 v14, v14, v67
	v_mul_f32_e32 v15, v15, v67
	v_cvt_pk_bf16_f32 v88, v4, v5
	v_cvt_pk_bf16_f32 v89, v6, v7
	v_cvt_pk_bf16_f32 v90, v12, v13
	v_cvt_pk_bf16_f32 v91, v14, v15
	s_nop 1
	v_permlane16_swap_b32_e32 v88, v90
	v_permlane16_swap_b32_e32 v89, v91
	s_nop 1
	global_store_dwordx4 v71, v[88:91], s[58:59] offset:0
	v_mul_f32_e32 v20, v20, v67
	v_mul_f32_e32 v21, v21, v67
	v_mul_f32_e32 v22, v22, v67
	v_mul_f32_e32 v23, v23, v67
	v_mul_f32_e32 v28, v28, v67
	v_mul_f32_e32 v29, v29, v67
	v_mul_f32_e32 v30, v30, v67
	v_mul_f32_e32 v31, v31, v67
	v_cvt_pk_bf16_f32 v92, v20, v21
	v_cvt_pk_bf16_f32 v93, v22, v23
	v_cvt_pk_bf16_f32 v94, v28, v29
	v_cvt_pk_bf16_f32 v95, v30, v31
	s_nop 1
	v_permlane16_swap_b32_e32 v92, v94
	v_permlane16_swap_b32_e32 v93, v95
	s_nop 1
	global_store_dwordx4 v71, v[92:95], s[58:59] offset:64
	v_mul_f32_e32 v36, v36, v67
	v_mul_f32_e32 v37, v37, v67
	v_mul_f32_e32 v38, v38, v67
	v_mul_f32_e32 v39, v39, v67
	v_mul_f32_e32 v44, v44, v67
	v_mul_f32_e32 v45, v45, v67
	v_mul_f32_e32 v46, v46, v67
	v_mul_f32_e32 v47, v47, v67
	v_cvt_pk_bf16_f32 v72, v36, v37
	v_cvt_pk_bf16_f32 v73, v38, v39
	v_cvt_pk_bf16_f32 v74, v44, v45
	v_cvt_pk_bf16_f32 v75, v46, v47
	s_nop 1
	v_permlane16_swap_b32_e32 v72, v74
	v_permlane16_swap_b32_e32 v73, v75
	s_nop 1
	global_store_dwordx4 v71, v[72:75], s[58:59] offset:128
	v_mul_f32_e32 v52, v52, v67
	v_mul_f32_e32 v53, v53, v67
	v_mul_f32_e32 v54, v54, v67
	v_mul_f32_e32 v55, v55, v67
	v_mul_f32_e32 v60, v60, v67
	v_mul_f32_e32 v61, v61, v67
	v_mul_f32_e32 v62, v62, v67
	v_mul_f32_e32 v63, v63, v67
	v_cvt_pk_bf16_f32 v76, v52, v53
	v_cvt_pk_bf16_f32 v77, v54, v55
	v_cvt_pk_bf16_f32 v78, v60, v61
	v_cvt_pk_bf16_f32 v79, v62, v63
	s_nop 1
	v_permlane16_swap_b32_e32 v76, v78
	v_permlane16_swap_b32_e32 v77, v79
	s_nop 1
	global_store_dwordx4 v71, v[76:79], s[58:59] offset:192
	s_barrier
